# attention: softmax tail (16 exp + 8 copies) hoisted into the last four P.V MFMA shadows of each half; rescale test shortened to an scc branch
# speedup vs baseline: 1.0087x; 1.0001x over previous
; template <bool FIRST> DEVI bool partialSM(f32x16& p0, f32x16& p1, float& m_reg, float& alpha) {
;     float pmax = p0[0];
; #pragma unroll
;     for (int r = 1; r < 16; ++r) pmax = fmaxf(pmax, p0[r]);
; #pragma unroll
;     for (int r = 0; r < 16; ++r) pmax = fmaxf(pmax, p1[r]);
;     { auto rr = __builtin_amdgcn_permlane32_swap(__float_as_uint(pmax), __float_as_uint(pmax), false, false);
;       pmax = fmaxf(__uint_as_float(rr[0]), __uint_as_float(rr[1])); }
;     if (FIRST) { m_reg = pmax; alpha = 1.f;
; #pragma unroll
;         for (int r = 0; r < 16; ++r) { p0[r] = __builtin_amdgcn_exp2f(p0[r] - pmax); p1[r] = p1[r] - pmax; }
;         return false;
;     } else if (__builtin_expect(__all(pmax <= ATT_THR), 1)) { alpha = 1.f;
; #pragma unroll
;         for (int r = 0; r < 16; ++r) p0[r] = __builtin_amdgcn_exp2f(p0[r]);
;         return false;
;     } else { const float d = fmaxf(pmax, 0.f); alpha = __builtin_amdgcn_exp2f(-d); m_reg += d;
; #pragma unroll
;         for (int r = 0; r < 16; ++r) { p0[r] = __builtin_amdgcn_exp2f(p0[r] - d); p1[r] = p1[r] - d; }
;         return true;
;     }
; }
; DEVI void finishSM(f32x16& p0, f32x16& p1, float alpha, float& l_reg, bf16x8& pa0, bf16x8& pa1, bf16x8& pa2, bf16x8& pa3) {
; #pragma unroll
;     for (int r = 0; r < 16; ++r) p1[r] = __builtin_amdgcn_exp2f(p1[r]);
;     f32x2 s2 = (f32x2){p0[0], p0[1]} + (f32x2){p1[0], p1[1]};
; #pragma unroll
;     for (int r = 2; r < 16; r += 2) s2 += (f32x2){p0[r], p0[r + 1]} + (f32x2){p1[r], p1[r + 1]};
;     float ps = s2[0] + s2[1];
;     { auto rr = __builtin_amdgcn_permlane32_swap(__float_as_uint(ps), __float_as_uint(ps), false, false);
;       ps = __uint_as_float(rr[0]) + __uint_as_float(rr[1]); }
;     l_reg = l_reg * alpha + ps;
;     ...
;     PK4(p0, 0, pa0); PK4(p0, 8, pa1); PK4(p1, 0, pa2); PK4(p1, 8, pa3);
;     ...
; }
; DEVI void qkt(f32x16& p0, f32x16& p1, const char* Kb, const bf16x8 (&qr)[6], int r32, int hi, const f32x16& cinit) {
; #pragma unroll
;     for (int d0 = 0; d0 < 6; ++d0) { const int cb = (d0 * 16 + hi * 8) * 2;
;         const bf16x8 k0 = *(const bf16x8*)(Kb + KSWZ(r32, cb)), k1 = *(const bf16x8*)(Kb + KSWZ(32 + r32, cb));
;         p0 = __builtin_amdgcn_mfma_f32_32x32x16_bf16(k0, qr[d0], d0 == 0 ? cinit : p0, 0, 0, 0);
;         p1 = __builtin_amdgcn_mfma_f32_32x32x16_bf16(k1, qr[d0], d0 == 0 ? cinit : p1, 0, 0, 0); }
; }
.LBB0_696:
	s_mul_i32 s6, s89, 0x6000
	s_add_i32 s6, s6, 0
	v_add_u32_e32 v86, s6, v129
	ds_read_b128 v[82:85], v86 offset:12288
	ds_read_b128 v[124:127], v86 offset:18432
	v_add_u32_e32 v174, s6, v204
	v_exp_f32_e32 v66, v66
	v_exp_f32_e32 v67, v67
	s_waitcnt lgkmcnt(0)
	v_mfma_f32_32x32x16_bf16 v[98:113], v[82:85], v[150:153], v[34:49]
	v_add_u32_e32 v82, s6, v184
	v_add_u32_e32 v83, s6, v185
	ds_read_b128 v[208:211], v82 offset:12288
	ds_read_b128 v[212:215], v82 offset:18432
	ds_read_b128 v[216:219], v83 offset:12288
	ds_read_b128 v[220:223], v83 offset:18432
	v_exp_f32_e32 v68, v68
	v_exp_f32_e32 v69, v69
	v_exp_f32_e32 v70, v70
	v_exp_f32_e32 v71, v71
	s_waitcnt lgkmcnt(4)
	v_mfma_f32_32x32x16_bf16 v[82:97], v[124:127], v[150:153], v[34:49]
	ds_read_b128 v[124:127], v174 offset:12288
	ds_read_b128 v[224:227], v174 offset:18432
	v_exp_f32_e32 v72, v72
	v_exp_f32_e32 v73, v73
	v_exp_f32_e32 v74, v74
	v_exp_f32_e32 v75, v75
	v_exp_f32_e32 v76, v76
	v_exp_f32_e32 v77, v77
	s_waitcnt lgkmcnt(0)
	v_mfma_f32_32x32x16_bf16 v[98:113], v[208:211], v[138:141], v[98:113]
	v_add_u32_e32 v174, s6, v205
	v_exp_f32_e32 v78, v78
	v_exp_f32_e32 v79, v79
	ds_read_b128 v[228:231], v174 offset:12288
	ds_read_b128 v[232:235], v174 offset:18432
	v_exp_f32_e32 v80, v80
	v_exp_f32_e32 v81, v81
	v_add_u32_e32 v174, s6, v206
	s_waitcnt lgkmcnt(6)
	v_mfma_f32_32x32x16_bf16 v[82:97], v[212:215], v[138:141], v[82:97]
	v_add_f32_e64 v212, v50, v66
	v_add_f32_e64 v213, v51, v67
	v_add_f32_e64 v214, v52, v68
	v_add_f32_e64 v215, v53, v69
	v_lshl_add_u32 v202, s89, 14, v115
	v_pk_add_f32 v[212:213], v[214:215], v[212:213]
	v_pk_add_f32 v[214:215], v[54:55], v[70:71]
	ds_read_b128 v[208:211], v174 offset:12288
	ds_read_b128 v[236:239], v174 offset:18432
	v_pk_add_f32 v[212:213], v[214:215], v[212:213]
	s_waitcnt lgkmcnt(7)
	v_mfma_f32_32x32x16_bf16 v[98:113], v[216:219], v[134:137], v[98:113]
	v_add_f32_e64 v214, v56, v72
	v_add_f32_e64 v215, v57, v73
	v_cvt_pk_bf16_f32 v50, v50, v51
	v_cvt_pk_bf16_f32 v51, v52, v53
	v_cvt_pk_bf16_f32 v52, v54, v55
	v_cvt_pk_bf16_f32 v53, v56, v57
	v_cvt_pk_bf16_f32 v54, v58, v59
	v_add_f32_e64 v212, v214, v212
	v_add_f32_e64 v213, v215, v213
	s_waitcnt lgkmcnt(6)
	v_mfma_f32_32x32x16_bf16 v[82:97], v[220:223], v[134:137], v[82:97]
	v_add_f32_e64 v214, v58, v74
	v_add_f32_e64 v215, v59, v75
	v_cvt_pk_bf16_f32 v55, v60, v61
	v_cvt_pk_bf16_f32 v56, v62, v63
	v_cvt_pk_bf16_f32 v57, v64, v65
	v_cvt_pk_bf16_f32 v58, v66, v67
	v_cvt_pk_bf16_f32 v59, v68, v69
	v_add_f32_e64 v212, v214, v212
	v_add_f32_e64 v213, v215, v213
	s_waitcnt lgkmcnt(5)
	v_mfma_f32_32x32x16_bf16 v[98:113], v[124:127], v[130:133], v[98:113]
	v_add_f32_e64 v214, v60, v76
	v_add_f32_e64 v215, v61, v77
	v_add_f32_e64 v126, v62, v78
	v_add_f32_e64 v127, v63, v79
	v_add_f32_e64 v124, v214, v212
	v_add_f32_e64 v125, v215, v213
	v_cvt_pk_bf16_f32 v60, v70, v71
	v_cvt_pk_bf16_f32 v61, v72, v73
	v_cvt_pk_bf16_f32 v62, v74, v75
	v_cvt_pk_bf16_f32 v63, v76, v77
	s_waitcnt lgkmcnt(4)
	v_mfma_f32_32x32x16_bf16 v[82:97], v[224:227], v[130:133], v[82:97]
	v_add_f32_e64 v124, v126, v124
	v_add_f32_e64 v125, v127, v125
	v_add_f32_e64 v126, v64, v80
	v_add_f32_e64 v127, v65, v81
	v_cvt_pk_bf16_f32 v64, v78, v79
	v_cvt_pk_bf16_f32 v65, v80, v81
	ds_read_b64_tr_b16 v[66:67], v202 offset:0
	ds_read_b64_tr_b16 v[68:69], v202 offset:0x400
	ds_read_b64_tr_b16 v[70:71], v202 offset:0x800
	s_waitcnt lgkmcnt(0)
	v_mfma_f32_32x32x16_bf16 v[98:113], v[228:231], v[146:149], v[98:113]
	ds_read_b64_tr_b16 v[72:73], v202 offset:0xc00
	ds_read_b64_tr_b16 v[74:75], v202 offset:0x1000
	ds_read_b64_tr_b16 v[76:77], v202 offset:0x1400
	ds_read_b64_tr_b16 v[78:79], v202 offset:0x1800
	ds_read_b64_tr_b16 v[80:81], v202 offset:0x1c00
	v_add_f32_e64 v124, v126, v124
	v_add_f32_e64 v125, v127, v125
	s_waitcnt lgkmcnt(2)
	v_mfma_f32_32x32x16_bf16 v[82:97], v[232:235], v[146:149], v[82:97]
	v_pk_add_f32 v[124:125], v[124:125], v[124:125] op_sel:[0,1] op_sel_hi:[1,0]
	s_nop 0
	v_mov_b32_e32 v125, v124
	s_nop 1
	v_permlane32_swap_b32_e32 v124, v125
	s_waitcnt lgkmcnt(1)
	v_mfma_f32_32x32x16_bf16 v[98:113], v[208:211], v[142:145], v[98:113]
	ds_read_b64_tr_b16 v[208:209], v202 offset:0x200
	ds_read_b64_tr_b16 v[210:211], v202 offset:0x600
	ds_read_b64_tr_b16 v[212:213], v202 offset:0xa00
	ds_read_b64_tr_b16 v[214:215], v202 offset:0xe00
	ds_read_b64_tr_b16 v[216:217], v202 offset:0x1200
	ds_read_b64_tr_b16 v[218:219], v202 offset:0x1600
	ds_read_b64_tr_b16 v[220:221], v202 offset:0x1a00
	s_waitcnt lgkmcnt(0)
	v_mfma_f32_32x32x16_bf16 v[82:97], v[236:239], v[142:145], v[82:97]
	ds_read_b64_tr_b16 v[222:223], v202 offset:0x1e00
	s_waitcnt lgkmcnt(8)
	v_mfma_f32_32x32x16_bf16 v[18:33], v[50:53], v[66:69], v[18:33]
	s_waitcnt lgkmcnt(0)
	v_mfma_f32_32x32x16_bf16 v[18:33], v[54:57], v[70:73], v[18:33]
	v_mfma_f32_32x32x16_bf16 v[18:33], v[58:61], v[74:77], v[18:33]
	v_mfma_f32_32x32x16_bf16 v[18:33], v[62:65], v[78:81], v[18:33]
	v_mfma_f32_32x32x16_bf16 v[2:17], v[50:53], v[208:211], v[2:17]
	s_nop 4
	v_max_f32_e32 v249, v99, v99
	v_max_f32_e32 v250, v98, v98
	v_max_f32_e32 v249, v250, v249
	v_max3_f32 v249, v249, v100, v101
	v_max3_f32 v249, v249, v102, v103
	v_max3_f32 v251, v249, v104, v105
	v_max3_f32 v251, v251, v106, v107
	v_exp_f32_e32 v50, v98
	v_exp_f32_e32 v51, v99
	v_exp_f32_e32 v52, v100
	v_exp_f32_e32 v53, v101
	v_mov_b64_e32 v[66:67], v[82:83]
	v_mov_b64_e32 v[68:69], v[84:85]
	v_mfma_f32_32x32x16_bf16 v[2:17], v[54:57], v[212:215], v[2:17]
	v_max3_f32 v251, v251, v108, v109
	v_max3_f32 v251, v251, v110, v111
	v_max3_f32 v251, v251, v112, v113
	v_max3_f32 v251, v251, v82, v83
	v_max3_f32 v251, v251, v84, v85
	v_max3_f32 v251, v251, v86, v87
	v_max3_f32 v251, v251, v88, v89
	v_exp_f32_e32 v54, v102
	v_exp_f32_e32 v55, v103
	v_exp_f32_e32 v56, v104
	v_exp_f32_e32 v57, v105
	v_mov_b64_e32 v[70:71], v[86:87]
	v_mov_b64_e32 v[72:73], v[88:89]
	v_mfma_f32_32x32x16_bf16 v[2:17], v[58:61], v[216:219], v[2:17]
	v_max3_f32 v251, v251, v90, v91
	v_max3_f32 v251, v251, v92, v93
	v_max3_f32 v251, v251, v94, v95
	v_max3_f32 v251, v251, v96, v97
	v_mov_b32_e32 v252, v251
	s_nop 1
	v_permlane32_swap_b32_e32 v251, v252
	v_exp_f32_e32 v58, v106
	v_exp_f32_e32 v59, v107
	v_exp_f32_e32 v60, v108
	v_exp_f32_e32 v61, v109
	v_mov_b64_e32 v[74:75], v[90:91]
	v_mov_b64_e32 v[76:77], v[92:93]
	v_mfma_f32_32x32x16_bf16 v[2:17], v[62:65], v[220:223], v[2:17]
	v_exp_f32_e32 v62, v110
	v_exp_f32_e32 v63, v111
	v_exp_f32_e32 v64, v112
	v_exp_f32_e32 v65, v113
	v_mov_b64_e32 v[78:79], v[94:95]
	v_mov_b64_e32 v[80:81], v[96:97]
	v_max_f32_e32 v252, v252, v252
	v_max_f32_e32 v251, v251, v251
	v_max_f32_e32 v126, v251, v252
	v_cmp_ge_f32_e32 vcc, s79, v126
	s_cmp_lg_u64 vcc, exec
	s_cselect_b64 s[6:7], -1, 0
	s_cbranch_scc1 .LBB0_705
	v_mov_b32_e32 v208, 1.0
	v_mov_b32_e32 v209, v203
	s_branch .LBB0_699

; DEVI void attn_unit8(const Params& p, char* smem, int unit, int l, int& cvs  , CvRun& crun) {
;     ...
;         __syncthreads();
;         if (T + 2 < NTILE) B_DMA(T + 2, s2);
.LBB0_702:
	s_mul_i32 s6, s2, 0x6000
	s_add_i32 s6, s96, s6
	v_lshl_add_u64 v[82:83], v[118:119], 0, s[12:13]
	s_mov_b32 m0, s6
	s_barrier
; template <bool FIRST> DEVI bool partialSM(f32x16& p0, f32x16& p1, float& m_reg, float& alpha) {
;     float pmax = p0[0];
; #pragma unroll
;     for (int r = 1; r < 16; ++r) pmax = fmaxf(pmax, p0[r]);
; #pragma unroll
;     for (int r = 0; r < 16; ++r) pmax = fmaxf(pmax, p1[r]);
;     { auto rr = __builtin_amdgcn_permlane32_swap(__float_as_uint(pmax), __float_as_uint(pmax), false, false);
;       pmax = fmaxf(__uint_as_float(rr[0]), __uint_as_float(rr[1])); }
;     if (FIRST) { m_reg = pmax; alpha = 1.f;
; #pragma unroll
;         for (int r = 0; r < 16; ++r) { p0[r] = __builtin_amdgcn_exp2f(p0[r] - pmax); p1[r] = p1[r] - pmax; }
;         return false;
;     } else if (__builtin_expect(__all(pmax <= ATT_THR), 1)) { alpha = 1.f;
; #pragma unroll
;         for (int r = 0; r < 16; ++r) p0[r] = __builtin_amdgcn_exp2f(p0[r]);
;         return false;
;     } else { const float d = fmaxf(pmax, 0.f); alpha = __builtin_amdgcn_exp2f(-d); m_reg += d;
; #pragma unroll
;         for (int r = 0; r < 16; ++r) { p0[r] = __builtin_amdgcn_exp2f(p0[r] - d); p1[r] = p1[r] - d; }
;         return true;
;     }
; }
; DEVI void finishSM(f32x16& p0, f32x16& p1, float alpha, float& l_reg, bf16x8& pa0, bf16x8& pa1, bf16x8& pa2, bf16x8& pa3) {
; #pragma unroll
;     for (int r = 0; r < 16; ++r) p1[r] = __builtin_amdgcn_exp2f(p1[r]);
;     f32x2 s2 = (f32x2){p0[0], p0[1]} + (f32x2){p1[0], p1[1]};
; #pragma unroll
;     for (int r = 2; r < 16; r += 2) s2 += (f32x2){p0[r], p0[r + 1]} + (f32x2){p1[r], p1[r + 1]};
;     float ps = s2[0] + s2[1];
;     { auto rr = __builtin_amdgcn_permlane32_swap(__float_as_uint(ps), __float_as_uint(ps), false, false);
;       ps = __uint_as_float(rr[0]) + __uint_as_float(rr[1]); }
;     l_reg = l_reg * alpha + ps;
;     ...
;     PK4(p0, 0, pa0); PK4(p0, 8, pa1); PK4(p1, 0, pa2); PK4(p1, 8, pa3);
;     ...
; }
; DEVI void qkt(f32x16& p0, f32x16& p1, const char* Kb, const bf16x8 (&qr)[6], int r32, int hi, const f32x16& cinit) {
; #pragma unroll
;     for (int d0 = 0; d0 < 6; ++d0) { const int cb = (d0 * 16 + hi * 8) * 2;
;         const bf16x8 k0 = *(const bf16x8*)(Kb + KSWZ(r32, cb)), k1 = *(const bf16x8*)(Kb + KSWZ(32 + r32, cb));
;         p0 = __builtin_amdgcn_mfma_f32_32x32x16_bf16(k0, qr[d0], d0 == 0 ? cinit : p0, 0, 0, 0);
;         p1 = __builtin_amdgcn_mfma_f32_32x32x16_bf16(k1, qr[d0], d0 == 0 ? cinit : p1, 0, 0, 0); }
; }
	global_load_lds_dwordx4 v[82:83], off
	v_lshl_add_u64 v[82:83], v[120:121], 0, s[12:13]
	s_add_i32 m0, s6, 0x2000
	v_exp_f32_e32 v66, v66
	global_load_lds_dwordx4 v[82:83], off
	s_add_i32 m0, s6, 0x4000
	s_lshl_b32 s6, s2, 14
	v_lshl_add_u64 v[82:83], v[122:123], 0, s[12:13]
	s_add_i32 s6, s97, s6
	global_load_lds_dwordx4 v[82:83], off
	s_mov_b32 m0, s6
	v_lshl_add_u64 v[82:83], v[116:117], 0, s[40:41]
	global_load_lds_dwordx4 v[116:117], off
	s_add_i32 m0, s6, 0x2000
	s_mul_i32 s6, s61, 0x6000
	global_load_lds_dwordx4 v[82:83], off
	s_add_i32 s6, s6, 0
	v_add_u32_e32 v86, s6, v129
	ds_read_b128 v[82:85], v86
	ds_read_b128 v[210:213], v86 offset:6144
	s_waitcnt lgkmcnt(0)
	v_mfma_f32_32x32x16_bf16 v[98:113], v[82:85], v[150:153], v[34:49]
	v_add_u32_e32 v126, s6, v184
	v_exp_f32_e32 v67, v67
	v_exp_f32_e32 v68, v68
	v_exp_f32_e32 v69, v69
	v_exp_f32_e32 v70, v70
	v_exp_f32_e32 v71, v71
	v_exp_f32_e32 v72, v72
	v_mfma_f32_32x32x16_bf16 v[82:97], v[210:213], v[150:153], v[34:49]
	ds_read_b128 v[210:213], v126
	ds_read_b128 v[214:217], v126 offset:6144
	v_add_u32_e32 v126, s6, v185
	v_exp_f32_e32 v73, v73
	v_exp_f32_e32 v74, v74
	v_exp_f32_e32 v75, v75
	v_exp_f32_e32 v76, v76
	v_exp_f32_e32 v77, v77
	s_waitcnt lgkmcnt(0)
	v_mfma_f32_32x32x16_bf16 v[98:113], v[210:213], v[138:141], v[98:113]
	v_exp_f32_e32 v78, v78
	v_exp_f32_e32 v79, v79
	v_exp_f32_e32 v80, v80
	v_exp_f32_e32 v81, v81
	v_add_u32_e32 v174, 0x2000, v202
	v_mfma_f32_32x32x16_bf16 v[82:97], v[214:217], v[138:141], v[82:97]
	ds_read_b128 v[210:213], v126
	ds_read_b128 v[214:217], v126 offset:6144
	v_add_u32_e32 v126, s6, v204
	s_waitcnt lgkmcnt(0)
	v_mfma_f32_32x32x16_bf16 v[98:113], v[210:213], v[134:137], v[98:113]
	ds_read_b128 v[210:213], v126
	ds_read_b128 v[218:221], v126 offset:6144
	v_add_u32_e32 v126, s6, v205
	v_mfma_f32_32x32x16_bf16 v[82:97], v[214:217], v[134:137], v[82:97]
	ds_read_b128 v[214:217], v126
	ds_read_b128 v[222:225], v126 offset:6144
	v_add_u32_e32 v126, s6, v206
	ds_read_b128 v[226:229], v126
	ds_read_b128 v[230:233], v126 offset:6144
	v_pk_add_f32 v[126:127], v[50:51], v[66:67]
	v_cvt_pk_bf16_f32 v50, v50, v51
	v_cvt_pk_bf16_f32 v51, v52, v53
	s_waitcnt lgkmcnt(0)
	v_mfma_f32_32x32x16_bf16 v[98:113], v[210:213], v[130:133], v[98:113]
	v_add_f32_e64 v210, v52, v68
	v_add_f32_e64 v211, v53, v69
	v_cvt_pk_bf16_f32 v52, v54, v55
	v_cvt_pk_bf16_f32 v53, v56, v57
	v_add_f32_e64 v126, v210, v126
	v_add_f32_e64 v127, v211, v127
	v_add_f32_e64 v210, v54, v70
	v_add_f32_e64 v211, v55, v71
	v_cvt_pk_bf16_f32 v54, v58, v59
	v_mfma_f32_32x32x16_bf16 v[82:97], v[218:221], v[130:133], v[82:97]
	v_add_f32_e64 v126, v210, v126
	v_add_f32_e64 v127, v211, v127
	v_add_f32_e64 v210, v56, v72
	v_add_f32_e64 v211, v57, v73
	v_cvt_pk_bf16_f32 v55, v60, v61
	v_cvt_pk_bf16_f32 v56, v62, v63
	v_cvt_pk_bf16_f32 v57, v64, v65
	v_add_f32_e64 v126, v210, v126
	v_add_f32_e64 v127, v211, v127
	v_pk_add_f32 v[210:211], v[58:59], v[74:75]
	v_cvt_pk_bf16_f32 v58, v66, v67
	v_cvt_pk_bf16_f32 v59, v68, v69
	v_mfma_f32_32x32x16_bf16 v[98:113], v[214:217], v[146:149], v[98:113]
	v_add_f32_e64 v126, v210, v126
	v_add_f32_e64 v127, v211, v127
	v_add_f32_e64 v210, v60, v76
	v_add_f32_e64 v211, v61, v77
	v_cvt_pk_bf16_f32 v60, v70, v71
	v_cvt_pk_bf16_f32 v61, v72, v73
	v_add_f32_e64 v126, v210, v126
	v_add_f32_e64 v127, v211, v127
	v_pk_add_f32 v[210:211], v[62:63], v[78:79]
	v_cvt_pk_bf16_f32 v62, v74, v75
	v_cvt_pk_bf16_f32 v63, v76, v77
	v_mfma_f32_32x32x16_bf16 v[82:97], v[222:225], v[146:149], v[82:97]
	v_add_f32_e64 v126, v210, v126
	v_add_f32_e64 v127, v211, v127
	v_add_f32_e64 v210, v64, v80
	v_add_f32_e64 v211, v65, v81
	v_cvt_pk_bf16_f32 v64, v78, v79
	v_cvt_pk_bf16_f32 v65, v80, v81
	ds_read_b64_tr_b16 v[66:67], v174 offset:0
	ds_read_b64_tr_b16 v[68:69], v174 offset:0x400
	ds_read_b64_tr_b16 v[70:71], v174 offset:0x800
	ds_read_b64_tr_b16 v[72:73], v174 offset:0xc00
	ds_read_b64_tr_b16 v[74:75], v174 offset:0x1000
	ds_read_b64_tr_b16 v[76:77], v174 offset:0x1400
	ds_read_b64_tr_b16 v[78:79], v174 offset:0x1800
	ds_read_b64_tr_b16 v[80:81], v174 offset:0x1c00
	v_add_f32_e64 v126, v210, v126
	v_add_f32_e64 v127, v211, v127
	ds_read_b64_tr_b16 v[210:211], v174 offset:0x200
	ds_read_b64_tr_b16 v[212:213], v174 offset:0x600
	ds_read_b64_tr_b16 v[214:215], v174 offset:0xa00
	v_mfma_f32_32x32x16_bf16 v[98:113], v[226:229], v[142:145], v[98:113]
	ds_read_b64_tr_b16 v[216:217], v174 offset:0xe00
	ds_read_b64_tr_b16 v[218:219], v174 offset:0x1200
	ds_read_b64_tr_b16 v[220:221], v174 offset:0x1600
	ds_read_b64_tr_b16 v[222:223], v174 offset:0x1a00
	ds_read_b64_tr_b16 v[224:225], v174 offset:0x1e00
	v_pk_add_f32 v[126:127], v[126:127], v[126:127] op_sel:[0,1] op_sel_hi:[1,0]
	s_waitcnt lgkmcnt(8)
	v_mfma_f32_32x32x16_bf16 v[82:97], v[230:233], v[142:145], v[82:97]
	v_mov_b32_e32 v127, v126
	s_nop 1
	v_permlane32_swap_b32_e32 v126, v127
	v_mfma_f32_32x32x16_bf16 v[18:33], v[50:53], v[66:69], v[18:33]
	s_waitcnt lgkmcnt(0)
	v_mfma_f32_32x32x16_bf16 v[18:33], v[54:57], v[70:73], v[18:33]
	v_mfma_f32_32x32x16_bf16 v[18:33], v[58:61], v[74:77], v[18:33]
	v_mfma_f32_32x32x16_bf16 v[18:33], v[62:65], v[78:81], v[18:33]
	v_mfma_f32_32x32x16_bf16 v[2:17], v[50:53], v[210:213], v[2:17]
	s_nop 0
	v_max_f32_e32 v249, v99, v99
	v_max_f32_e32 v250, v98, v98
	v_max_f32_e32 v249, v250, v249
	v_max3_f32 v249, v249, v100, v101
	v_max3_f32 v249, v249, v102, v103
	v_max3_f32 v251, v249, v104, v105
	v_max3_f32 v251, v251, v106, v107
	v_exp_f32_e32 v50, v98
	v_exp_f32_e32 v51, v99
	v_exp_f32_e32 v52, v100
	v_exp_f32_e32 v53, v101
	v_mov_b64_e32 v[66:67], v[82:83]
	v_mov_b64_e32 v[68:69], v[84:85]
	v_mfma_f32_32x32x16_bf16 v[2:17], v[54:57], v[214:217], v[2:17]
	v_max3_f32 v251, v251, v108, v109
	v_max3_f32 v251, v251, v110, v111
	v_max3_f32 v251, v251, v112, v113
	v_max3_f32 v251, v251, v82, v83
	v_max3_f32 v251, v251, v84, v85
	v_max3_f32 v251, v251, v86, v87
	v_max3_f32 v251, v251, v88, v89
	v_exp_f32_e32 v54, v102
	v_exp_f32_e32 v55, v103
	v_exp_f32_e32 v56, v104
	v_exp_f32_e32 v57, v105
	v_mov_b64_e32 v[70:71], v[86:87]
	v_mov_b64_e32 v[72:73], v[88:89]
	v_mfma_f32_32x32x16_bf16 v[2:17], v[58:61], v[218:221], v[2:17]
	v_max3_f32 v251, v251, v90, v91
	v_max3_f32 v251, v251, v92, v93
	v_max3_f32 v251, v251, v94, v95
	v_max3_f32 v251, v251, v96, v97
	v_mov_b32_e32 v252, v251
	s_nop 1
	v_permlane32_swap_b32_e32 v251, v252
	v_exp_f32_e32 v58, v106
	v_exp_f32_e32 v59, v107
	v_exp_f32_e32 v60, v108
	v_exp_f32_e32 v61, v109
	v_mov_b64_e32 v[74:75], v[90:91]
	v_mov_b64_e32 v[76:77], v[92:93]
	v_mfma_f32_32x32x16_bf16 v[2:17], v[62:65], v[222:225], v[2:17]
	v_exp_f32_e32 v62, v110
	v_exp_f32_e32 v63, v111
	v_exp_f32_e32 v64, v112
	v_exp_f32_e32 v65, v113
	v_mov_b64_e32 v[78:79], v[94:95]
	v_mov_b64_e32 v[80:81], v[96:97]
	v_max_f32_e32 v252, v252, v252
	v_max_f32_e32 v251, v251, v251
	v_max_f32_e32 v174, v251, v252
	v_cmp_ge_f32_e32 vcc, s79, v174
	s_cmp_lg_u64 vcc, exec
	s_cselect_b64 s[6:7], -1, 0
	s_cbranch_scc1 .LBB0_711
	v_mov_b32_e32 v202, 1.0
	v_mov_b32_e32 v203, v209
	s_branch .LBB0_716

; template <bool FIRST> DEVI bool partialSM(f32x16& p0, f32x16& p1, float& m_reg, float& alpha) {
;     ...
;     } else { const float d = fmaxf(pmax, 0.f); alpha = __builtin_amdgcn_exp2f(-d); m_reg += d;
; #pragma unroll
;         for (int r = 0; r < 16; ++r) { p0[r] = __builtin_amdgcn_exp2f(p0[r] - d); p1[r] = p1[r] - d; }
;         return true;
;     }
.LBB0_705:
	v_max_f32_e32 v50, v126, v126
	v_max_f32_e32 v66, 0, v50
	v_sub_f32_e32 v50, v98, v66
	v_sub_f32_e32 v51, v99, v66
	v_sub_f32_e32 v52, v100, v66
	v_sub_f32_e32 v53, v101, v66
	v_sub_f32_e32 v54, v102, v66
	v_sub_f32_e32 v55, v103, v66
	v_sub_f32_e32 v56, v104, v66
	v_sub_f32_e32 v57, v105, v66
	v_sub_f32_e32 v58, v106, v66
	v_sub_f32_e32 v59, v107, v66
	v_sub_f32_e32 v60, v108, v66
	v_sub_f32_e32 v61, v109, v66
	v_sub_f32_e32 v62, v110, v66
	v_sub_f32_e32 v63, v111, v66
	v_sub_f32_e32 v64, v112, v66
	v_sub_f32_e32 v65, v113, v66
	v_exp_f32_e64 v208, -v66
	v_add_f32_e32 v209, v203, v66
	v_exp_f32_e32 v50, v50
	v_exp_f32_e32 v51, v51
	v_exp_f32_e32 v52, v52
	v_exp_f32_e32 v53, v53
	v_exp_f32_e32 v54, v54
	v_exp_f32_e32 v55, v55
	v_exp_f32_e32 v56, v56
	v_exp_f32_e32 v57, v57
	v_exp_f32_e32 v58, v58
	v_exp_f32_e32 v59, v59
	v_exp_f32_e32 v60, v60
	v_exp_f32_e32 v61, v61
	v_exp_f32_e32 v62, v62
	v_exp_f32_e32 v63, v63
	v_exp_f32_e32 v64, v64
	v_exp_f32_e32 v65, v65
	v_sub_f32_e32 v81, v97, v66
	v_sub_f32_e32 v80, v96, v66
	v_sub_f32_e32 v79, v95, v66
	v_sub_f32_e32 v78, v94, v66
	v_sub_f32_e32 v77, v93, v66
	v_sub_f32_e32 v76, v92, v66
	v_sub_f32_e32 v75, v91, v66
	v_sub_f32_e32 v74, v90, v66
	v_sub_f32_e32 v73, v89, v66
	v_sub_f32_e32 v72, v88, v66
	v_sub_f32_e32 v71, v87, v66
	v_sub_f32_e32 v70, v86, v66
	v_sub_f32_e32 v69, v85, v66
	v_sub_f32_e32 v68, v84, v66
	v_sub_f32_e32 v67, v83, v66
	v_sub_f32_e32 v66, v82, v66
	s_cbranch_execnz .LBB0_698
.LBB0_707:
	s_and_saveexec_b64 s[6:7], s[4:5]
	ds_write_b32 v187, v208 offset:128
	s_or_b64 exec, exec, s[6:7]
	v_add_u32_e32 v46, s91, v178
	s_waitcnt lgkmcnt(0)
	ds_read_b128 v[34:37], v46 offset:224
	ds_read_b128 v[38:41], v46 offset:192
	ds_read_b128 v[42:45], v46 offset:160
	ds_read_b128 v[46:49], v46 offset:128
	s_waitcnt lgkmcnt(0)
	v_pk_mul_f32 v[30:31], v[30:31], v[34:35]
	v_pk_mul_f32 v[14:15], v[14:15], v[34:35]
	v_xor_b32_e32 v34, 0x80000000, v209
	s_waitcnt lgkmcnt(2)
	v_pk_mul_f32 v[26:27], v[26:27], v[38:39]
	s_waitcnt lgkmcnt(1)
	v_pk_mul_f32 v[22:23], v[22:23], v[42:43]
	v_pk_mul_f32 v[32:33], v[32:33], v[36:37]
	v_pk_mul_f32 v[28:29], v[28:29], v[40:41]
	v_pk_mul_f32 v[24:25], v[24:25], v[44:45]
	s_waitcnt lgkmcnt(0)
	v_pk_mul_f32 v[20:21], v[20:21], v[48:49]
	v_pk_mul_f32 v[18:19], v[18:19], v[46:47]
	v_pk_mul_f32 v[10:11], v[10:11], v[38:39]
	v_pk_mul_f32 v[6:7], v[6:7], v[42:43]
	v_pk_mul_f32 v[16:17], v[16:17], v[36:37]
	v_pk_mul_f32 v[12:13], v[12:13], v[40:41]
	v_pk_mul_f32 v[8:9], v[8:9], v[44:45]
	v_pk_mul_f32 v[4:5], v[4:5], v[48:49]
	v_pk_mul_f32 v[2:3], v[2:3], v[46:47]
	v_mov_b32_e32 v35, v34
	v_mov_b32_e32 v36, v34
	v_mov_b32_e32 v37, v34
	v_mov_b32_e32 v38, v34
	v_mov_b32_e32 v39, v34
	v_mov_b32_e32 v40, v34
	v_mov_b32_e32 v41, v34
	v_mov_b32_e32 v42, v34
	v_mov_b32_e32 v43, v34
	v_mov_b32_e32 v44, v34
	v_mov_b32_e32 v45, v34
	v_mov_b32_e32 v46, v34
	v_mov_b32_e32 v47, v34
	v_mov_b32_e32 v48, v34
	v_mov_b32_e32 v49, v34
	s_andn2_b64 vcc, exec, s[14:15]
	s_mov_b64 s[6:7], -1
	s_cbranch_vccnz .LBB0_700

; template <bool FIRST> DEVI bool partialSM(f32x16& p0, f32x16& p1, float& m_reg, float& alpha) {
;     ...
;     } else { const float d = fmaxf(pmax, 0.f); alpha = __builtin_amdgcn_exp2f(-d); m_reg += d;
; #pragma unroll
;         for (int r = 0; r < 16; ++r) { p0[r] = __builtin_amdgcn_exp2f(p0[r] - d); p1[r] = p1[r] - d; }
;         return true;
;     }
.LBB0_711:
	v_max_f32_e32 v50, v174, v174
	v_max_f32_e32 v66, 0, v50
	v_sub_f32_e32 v50, v98, v66
	v_sub_f32_e32 v51, v99, v66
	v_sub_f32_e32 v52, v100, v66
	v_sub_f32_e32 v53, v101, v66
	v_sub_f32_e32 v54, v102, v66
	v_sub_f32_e32 v55, v103, v66
	v_sub_f32_e32 v56, v104, v66
	v_sub_f32_e32 v57, v105, v66
	v_sub_f32_e32 v58, v106, v66
	v_sub_f32_e32 v59, v107, v66
	v_sub_f32_e32 v60, v108, v66
	v_sub_f32_e32 v61, v109, v66
	v_sub_f32_e32 v62, v110, v66
	v_sub_f32_e32 v63, v111, v66
	v_sub_f32_e32 v64, v112, v66
	v_sub_f32_e32 v65, v113, v66
	v_exp_f32_e64 v202, -v66
	v_add_f32_e32 v203, v209, v66
	v_exp_f32_e32 v50, v50
	v_exp_f32_e32 v51, v51
	v_exp_f32_e32 v52, v52
	v_exp_f32_e32 v53, v53
	v_exp_f32_e32 v54, v54
	v_exp_f32_e32 v55, v55
	v_exp_f32_e32 v56, v56
	v_exp_f32_e32 v57, v57
	v_exp_f32_e32 v58, v58
	v_exp_f32_e32 v59, v59
	v_exp_f32_e32 v60, v60
	v_exp_f32_e32 v61, v61
	v_exp_f32_e32 v62, v62
	v_exp_f32_e32 v63, v63
	v_exp_f32_e32 v64, v64
	v_exp_f32_e32 v65, v65
	v_sub_f32_e32 v81, v97, v66
	v_sub_f32_e32 v80, v96, v66
	v_sub_f32_e32 v79, v95, v66
	v_sub_f32_e32 v78, v94, v66
	v_sub_f32_e32 v77, v93, v66
	v_sub_f32_e32 v76, v92, v66
	v_sub_f32_e32 v75, v91, v66
	v_sub_f32_e32 v74, v90, v66
	v_sub_f32_e32 v73, v89, v66
	v_sub_f32_e32 v72, v88, v66
	v_sub_f32_e32 v71, v87, v66
	v_sub_f32_e32 v70, v86, v66
	v_sub_f32_e32 v69, v85, v66
	v_sub_f32_e32 v68, v84, v66
	v_sub_f32_e32 v67, v83, v66
	v_sub_f32_e32 v66, v82, v66
	s_cbranch_execnz .LBB0_704
.LBB0_713:
	s_and_saveexec_b64 s[6:7], s[4:5]
	ds_write_b32 v187, v202 offset:128
	s_or_b64 exec, exec, s[6:7]
	v_add_u32_e32 v46, s91, v178
	s_waitcnt lgkmcnt(0)
	ds_read_b128 v[34:37], v46 offset:224
	ds_read_b128 v[38:41], v46 offset:192
	ds_read_b128 v[42:45], v46 offset:160
	ds_read_b128 v[46:49], v46 offset:128
	s_waitcnt lgkmcnt(0)
	v_pk_mul_f32 v[30:31], v[30:31], v[34:35]
	v_pk_mul_f32 v[14:15], v[14:15], v[34:35]
	v_xor_b32_e32 v34, 0x80000000, v203
	v_pk_mul_f32 v[26:27], v[26:27], v[38:39]
	v_pk_mul_f32 v[22:23], v[22:23], v[42:43]
	v_pk_mul_f32 v[32:33], v[32:33], v[36:37]
	v_pk_mul_f32 v[28:29], v[28:29], v[40:41]
	v_pk_mul_f32 v[24:25], v[24:25], v[44:45]
	v_pk_mul_f32 v[20:21], v[20:21], v[48:49]
	v_pk_mul_f32 v[18:19], v[18:19], v[46:47]
	v_pk_mul_f32 v[10:11], v[10:11], v[38:39]
	v_pk_mul_f32 v[6:7], v[6:7], v[42:43]
	v_pk_mul_f32 v[16:17], v[16:17], v[36:37]
	v_pk_mul_f32 v[12:13], v[12:13], v[40:41]
	v_pk_mul_f32 v[8:9], v[8:9], v[44:45]
	v_pk_mul_f32 v[4:5], v[4:5], v[48:49]
	v_pk_mul_f32 v[2:3], v[2:3], v[46:47]
	v_mov_b32_e32 v35, v34
	v_mov_b32_e32 v36, v34
	v_mov_b32_e32 v37, v34
	v_mov_b32_e32 v38, v34
	v_mov_b32_e32 v39, v34
	v_mov_b32_e32 v40, v34
	v_mov_b32_e32 v41, v34
	v_mov_b32_e32 v42, v34
	v_mov_b32_e32 v43, v34
	v_mov_b32_e32 v44, v34
	v_mov_b32_e32 v45, v34
	v_mov_b32_e32 v46, v34
	v_mov_b32_e32 v47, v34
	v_mov_b32_e32 v48, v34
	v_mov_b32_e32 v49, v34

; template <bool FIRST> DEVI bool partialSM(f32x16& p0, f32x16& p1, float& m_reg, float& alpha) {
;     float pmax = p0[0];
; #pragma unroll
;     for (int r = 1; r < 16; ++r) pmax = fmaxf(pmax, p0[r]);
; #pragma unroll
;     for (int r = 0; r < 16; ++r) pmax = fmaxf(pmax, p1[r]);
;     { auto rr = __builtin_amdgcn_permlane32_swap(__float_as_uint(pmax), __float_as_uint(pmax), false, false);
;       pmax = fmaxf(__uint_as_float(rr[0]), __uint_as_float(rr[1])); }
;     if (FIRST) { m_reg = pmax; alpha = 1.f;
; #pragma unroll
;         for (int r = 0; r < 16; ++r) { p0[r] = __builtin_amdgcn_exp2f(p0[r] - pmax); p1[r] = p1[r] - pmax; }
;         return false;
;     } else if (__builtin_expect(__all(pmax <= ATT_THR), 1)) { alpha = 1.f;
; #pragma unroll
;         for (int r = 0; r < 16; ++r) p0[r] = __builtin_amdgcn_exp2f(p0[r]);
;         return false;
;     } else { const float d = fmaxf(pmax, 0.f); alpha = __builtin_amdgcn_exp2f(-d); m_reg += d;
; #pragma unroll
;         for (int r = 0; r < 16; ++r) { p0[r] = __builtin_amdgcn_exp2f(p0[r] - d); p1[r] = p1[r] - d; }
;         return true;
;     }
; }
; DEVI void finishSM(f32x16& p0, f32x16& p1, float alpha, float& l_reg, bf16x8& pa0, bf16x8& pa1, bf16x8& pa2, bf16x8& pa3) {
; #pragma unroll
;     for (int r = 0; r < 16; ++r) p1[r] = __builtin_amdgcn_exp2f(p1[r]);
;     f32x2 s2 = (f32x2){p0[0], p0[1]} + (f32x2){p1[0], p1[1]};
; #pragma unroll
;     for (int r = 2; r < 16; r += 2) s2 += (f32x2){p0[r], p0[r + 1]} + (f32x2){p1[r], p1[r + 1]};
;     float ps = s2[0] + s2[1];
;     { auto rr = __builtin_amdgcn_permlane32_swap(__float_as_uint(ps), __float_as_uint(ps), false, false);
;       ps = __uint_as_float(rr[0]) + __uint_as_float(rr[1]); }
;     l_reg = l_reg * alpha + ps;
;     ...
;     PK4(p0, 0, pa0); PK4(p0, 8, pa1); PK4(p1, 0, pa2); PK4(p1, 8, pa3);
;     ...
; }
; DEVI void qkt(f32x16& p0, f32x16& p1, const char* Kb, const bf16x8 (&qr)[6], int r32, int hi, const f32x16& cinit) {
; #pragma unroll
;     for (int d0 = 0; d0 < 6; ++d0) { const int cb = (d0 * 16 + hi * 8) * 2;
;         const bf16x8 k0 = *(const bf16x8*)(Kb + KSWZ(r32, cb)), k1 = *(const bf16x8*)(Kb + KSWZ(32 + r32, cb));
;         p0 = __builtin_amdgcn_mfma_f32_32x32x16_bf16(k0, qr[d0], d0 == 0 ? cinit : p0, 0, 0, 0);
;         p1 = __builtin_amdgcn_mfma_f32_32x32x16_bf16(k1, qr[d0], d0 == 0 ? cinit : p1, 0, 0, 0); }
; }
.LBB0_2260:
	s_mul_i32 s6, s71, 0x6000
	s_add_i32 s6, s6, 0
	v_add_u32_e32 v86, s6, v129
	ds_read_b128 v[82:85], v86 offset:12288
	ds_read_b128 v[124:127], v86 offset:18432
	v_add_u32_e32 v174, s6, v205
	v_exp_f32_e32 v66, v66
	v_exp_f32_e32 v67, v67
	s_waitcnt lgkmcnt(0)
	v_mfma_f32_32x32x16_bf16 v[98:113], v[82:85], v[150:153], v[34:49]
	v_add_u32_e32 v82, s6, v184
	v_add_u32_e32 v83, s6, v185
	ds_read_b128 v[210:213], v82 offset:12288
	ds_read_b128 v[214:217], v82 offset:18432
	ds_read_b128 v[218:221], v83 offset:12288
	ds_read_b128 v[222:225], v83 offset:18432
	v_exp_f32_e32 v68, v68
	v_exp_f32_e32 v69, v69
	v_exp_f32_e32 v70, v70
	v_exp_f32_e32 v71, v71
	s_waitcnt lgkmcnt(4)
	v_mfma_f32_32x32x16_bf16 v[82:97], v[124:127], v[150:153], v[34:49]
	ds_read_b128 v[124:127], v174 offset:12288
	ds_read_b128 v[226:229], v174 offset:18432
	v_exp_f32_e32 v72, v72
	v_exp_f32_e32 v73, v73
	v_exp_f32_e32 v74, v74
	v_exp_f32_e32 v75, v75
	v_exp_f32_e32 v76, v76
	v_exp_f32_e32 v77, v77
	s_waitcnt lgkmcnt(0)
	v_mfma_f32_32x32x16_bf16 v[98:113], v[210:213], v[138:141], v[98:113]
	v_add_u32_e32 v174, s6, v206
	v_exp_f32_e32 v78, v78
	v_exp_f32_e32 v79, v79
	ds_read_b128 v[230:233], v174 offset:12288
	ds_read_b128 v[234:237], v174 offset:18432
	v_exp_f32_e32 v80, v80
	v_exp_f32_e32 v81, v81
	v_add_u32_e32 v174, s6, v207
	s_waitcnt lgkmcnt(6)
	v_mfma_f32_32x32x16_bf16 v[82:97], v[214:217], v[138:141], v[82:97]
	v_add_f32_e64 v214, v50, v66
	v_add_f32_e64 v215, v51, v67
	v_add_f32_e64 v216, v52, v68
	v_add_f32_e64 v217, v53, v69
	v_lshl_add_u32 v203, s71, 14, v115
	v_pk_add_f32 v[214:215], v[216:217], v[214:215]
	v_pk_add_f32 v[216:217], v[54:55], v[70:71]
	ds_read_b128 v[210:213], v174 offset:12288
	ds_read_b128 v[238:241], v174 offset:18432
	v_pk_add_f32 v[214:215], v[216:217], v[214:215]
	s_waitcnt lgkmcnt(7)
	v_mfma_f32_32x32x16_bf16 v[98:113], v[218:221], v[134:137], v[98:113]
	v_add_f32_e64 v216, v56, v72
	v_add_f32_e64 v217, v57, v73
	v_cvt_pk_bf16_f32 v50, v50, v51
	v_cvt_pk_bf16_f32 v51, v52, v53
	v_cvt_pk_bf16_f32 v52, v54, v55
	v_cvt_pk_bf16_f32 v53, v56, v57
	v_cvt_pk_bf16_f32 v54, v58, v59
	v_add_f32_e64 v214, v216, v214
	v_add_f32_e64 v215, v217, v215
	s_waitcnt lgkmcnt(6)
	v_mfma_f32_32x32x16_bf16 v[82:97], v[222:225], v[134:137], v[82:97]
	v_add_f32_e64 v216, v58, v74
	v_add_f32_e64 v217, v59, v75
	v_cvt_pk_bf16_f32 v55, v60, v61
	v_cvt_pk_bf16_f32 v56, v62, v63
	v_cvt_pk_bf16_f32 v57, v64, v65
	v_cvt_pk_bf16_f32 v58, v66, v67
	v_cvt_pk_bf16_f32 v59, v68, v69
	v_add_f32_e64 v214, v216, v214
	v_add_f32_e64 v215, v217, v215
	s_waitcnt lgkmcnt(5)
	v_mfma_f32_32x32x16_bf16 v[98:113], v[124:127], v[130:133], v[98:113]
	v_add_f32_e64 v216, v60, v76
	v_add_f32_e64 v217, v61, v77
	v_add_f32_e64 v126, v62, v78
	v_add_f32_e64 v127, v63, v79
	v_add_f32_e64 v124, v216, v214
	v_add_f32_e64 v125, v217, v215
	v_cvt_pk_bf16_f32 v60, v70, v71
	v_cvt_pk_bf16_f32 v61, v72, v73
	v_cvt_pk_bf16_f32 v62, v74, v75
	v_cvt_pk_bf16_f32 v63, v76, v77
	s_waitcnt lgkmcnt(4)
	v_mfma_f32_32x32x16_bf16 v[82:97], v[226:229], v[130:133], v[82:97]
	v_add_f32_e64 v124, v126, v124
	v_add_f32_e64 v125, v127, v125
	v_add_f32_e64 v126, v64, v80
	v_add_f32_e64 v127, v65, v81
	v_cvt_pk_bf16_f32 v64, v78, v79
	v_cvt_pk_bf16_f32 v65, v80, v81
	ds_read_b64_tr_b16 v[66:67], v203 offset:0
	ds_read_b64_tr_b16 v[68:69], v203 offset:0x400
	ds_read_b64_tr_b16 v[70:71], v203 offset:0x800
	s_waitcnt lgkmcnt(0)
	v_mfma_f32_32x32x16_bf16 v[98:113], v[230:233], v[146:149], v[98:113]
	ds_read_b64_tr_b16 v[72:73], v203 offset:0xc00
	ds_read_b64_tr_b16 v[74:75], v203 offset:0x1000
	ds_read_b64_tr_b16 v[76:77], v203 offset:0x1400
	ds_read_b64_tr_b16 v[78:79], v203 offset:0x1800
	ds_read_b64_tr_b16 v[80:81], v203 offset:0x1c00
	v_add_f32_e64 v124, v126, v124
	v_add_f32_e64 v125, v127, v125
	s_waitcnt lgkmcnt(2)
	v_mfma_f32_32x32x16_bf16 v[82:97], v[234:237], v[146:149], v[82:97]
	v_pk_add_f32 v[124:125], v[124:125], v[124:125] op_sel:[0,1] op_sel_hi:[1,0]
	s_nop 0
	v_mov_b32_e32 v125, v124
	s_nop 1
	v_permlane32_swap_b32_e32 v124, v125
	s_waitcnt lgkmcnt(1)
	v_mfma_f32_32x32x16_bf16 v[98:113], v[210:213], v[142:145], v[98:113]
	ds_read_b64_tr_b16 v[210:211], v203 offset:0x200
	ds_read_b64_tr_b16 v[212:213], v203 offset:0x600
	ds_read_b64_tr_b16 v[214:215], v203 offset:0xa00
	ds_read_b64_tr_b16 v[216:217], v203 offset:0xe00
	ds_read_b64_tr_b16 v[218:219], v203 offset:0x1200
	ds_read_b64_tr_b16 v[220:221], v203 offset:0x1600
	ds_read_b64_tr_b16 v[222:223], v203 offset:0x1a00
	s_waitcnt lgkmcnt(0)
	v_mfma_f32_32x32x16_bf16 v[82:97], v[238:241], v[142:145], v[82:97]
	ds_read_b64_tr_b16 v[224:225], v203 offset:0x1e00
	s_waitcnt lgkmcnt(8)
	v_mfma_f32_32x32x16_bf16 v[18:33], v[50:53], v[66:69], v[18:33]
	s_waitcnt lgkmcnt(0)
	v_mfma_f32_32x32x16_bf16 v[18:33], v[54:57], v[70:73], v[18:33]
	v_mfma_f32_32x32x16_bf16 v[18:33], v[58:61], v[74:77], v[18:33]
	v_mfma_f32_32x32x16_bf16 v[18:33], v[62:65], v[78:81], v[18:33]
	v_mfma_f32_32x32x16_bf16 v[2:17], v[50:53], v[210:213], v[2:17]
	s_nop 4
	v_max_f32_e32 v249, v99, v99
	v_max_f32_e32 v250, v98, v98
	v_max_f32_e32 v249, v250, v249
	v_max3_f32 v249, v249, v100, v101
	v_max3_f32 v249, v249, v102, v103
	v_max3_f32 v251, v249, v104, v105
	v_max3_f32 v251, v251, v106, v107
	v_exp_f32_e32 v50, v98
	v_exp_f32_e32 v51, v99
	v_exp_f32_e32 v52, v100
	v_exp_f32_e32 v53, v101
	v_mov_b64_e32 v[66:67], v[82:83]
	v_mov_b64_e32 v[68:69], v[84:85]
	v_mfma_f32_32x32x16_bf16 v[2:17], v[54:57], v[214:217], v[2:17]
	v_max3_f32 v251, v251, v108, v109
	v_max3_f32 v251, v251, v110, v111
	v_max3_f32 v251, v251, v112, v113
	v_max3_f32 v251, v251, v82, v83
	v_max3_f32 v251, v251, v84, v85
	v_max3_f32 v251, v251, v86, v87
	v_max3_f32 v251, v251, v88, v89
	v_exp_f32_e32 v54, v102
	v_exp_f32_e32 v55, v103
	v_exp_f32_e32 v56, v104
	v_exp_f32_e32 v57, v105
	v_mov_b64_e32 v[70:71], v[86:87]
	v_mov_b64_e32 v[72:73], v[88:89]
	v_mfma_f32_32x32x16_bf16 v[2:17], v[58:61], v[218:221], v[2:17]
	v_max3_f32 v251, v251, v90, v91
	v_max3_f32 v251, v251, v92, v93
	v_max3_f32 v251, v251, v94, v95
	v_max3_f32 v251, v251, v96, v97
	v_mov_b32_e32 v252, v251
	s_nop 1
	v_permlane32_swap_b32_e32 v251, v252
	v_exp_f32_e32 v58, v106
	v_exp_f32_e32 v59, v107
	v_exp_f32_e32 v60, v108
	v_exp_f32_e32 v61, v109
	v_mov_b64_e32 v[74:75], v[90:91]
	v_mov_b64_e32 v[76:77], v[92:93]
	v_mfma_f32_32x32x16_bf16 v[2:17], v[62:65], v[222:225], v[2:17]
	v_exp_f32_e32 v62, v110
	v_exp_f32_e32 v63, v111
	v_exp_f32_e32 v64, v112
	v_exp_f32_e32 v65, v113
	v_mov_b64_e32 v[78:79], v[94:95]
	v_mov_b64_e32 v[80:81], v[96:97]
	v_max_f32_e32 v252, v252, v252
	v_max_f32_e32 v251, v251, v251
	v_max_f32_e32 v126, v251, v252
	v_cmp_ge_f32_e32 vcc, s80, v126
	s_cmp_lg_u64 vcc, exec
	s_cselect_b64 s[6:7], -1, 0
	s_cbranch_scc1 .LBB0_2269
	v_mov_b32_e32 v209, 1.0
	v_mov_b32_e32 v210, v204
	s_branch .LBB0_2263

; DEVI void attn_unit8(const Params& p, char* smem, int unit, int l, int& cvs  , CvRun& crun) {
;     ...
;         __syncthreads();
;         if (T + 2 < NTILE) B_DMA(T + 2, s2);
.LBB0_2266:
	s_mul_i32 s6, s61, 0x6000
	s_add_i32 s6, s96, s6
	v_lshl_add_u64 v[82:83], v[118:119], 0, s[12:13]
	s_mov_b32 m0, s6
	s_barrier
; template <bool FIRST> DEVI bool partialSM(f32x16& p0, f32x16& p1, float& m_reg, float& alpha) {
;     float pmax = p0[0];
; #pragma unroll
;     for (int r = 1; r < 16; ++r) pmax = fmaxf(pmax, p0[r]);
; #pragma unroll
;     for (int r = 0; r < 16; ++r) pmax = fmaxf(pmax, p1[r]);
;     { auto rr = __builtin_amdgcn_permlane32_swap(__float_as_uint(pmax), __float_as_uint(pmax), false, false);
;       pmax = fmaxf(__uint_as_float(rr[0]), __uint_as_float(rr[1])); }
;     if (FIRST) { m_reg = pmax; alpha = 1.f;
; #pragma unroll
;         for (int r = 0; r < 16; ++r) { p0[r] = __builtin_amdgcn_exp2f(p0[r] - pmax); p1[r] = p1[r] - pmax; }
;         return false;
;     } else if (__builtin_expect(__all(pmax <= ATT_THR), 1)) { alpha = 1.f;
; #pragma unroll
;         for (int r = 0; r < 16; ++r) p0[r] = __builtin_amdgcn_exp2f(p0[r]);
;         return false;
;     } else { const float d = fmaxf(pmax, 0.f); alpha = __builtin_amdgcn_exp2f(-d); m_reg += d;
; #pragma unroll
;         for (int r = 0; r < 16; ++r) { p0[r] = __builtin_amdgcn_exp2f(p0[r] - d); p1[r] = p1[r] - d; }
;         return true;
;     }
; }
; DEVI void finishSM(f32x16& p0, f32x16& p1, float alpha, float& l_reg, bf16x8& pa0, bf16x8& pa1, bf16x8& pa2, bf16x8& pa3) {
; #pragma unroll
;     for (int r = 0; r < 16; ++r) p1[r] = __builtin_amdgcn_exp2f(p1[r]);
;     f32x2 s2 = (f32x2){p0[0], p0[1]} + (f32x2){p1[0], p1[1]};
; #pragma unroll
;     for (int r = 2; r < 16; r += 2) s2 += (f32x2){p0[r], p0[r + 1]} + (f32x2){p1[r], p1[r + 1]};
;     float ps = s2[0] + s2[1];
;     { auto rr = __builtin_amdgcn_permlane32_swap(__float_as_uint(ps), __float_as_uint(ps), false, false);
;       ps = __uint_as_float(rr[0]) + __uint_as_float(rr[1]); }
;     l_reg = l_reg * alpha + ps;
;     ...
;     PK4(p0, 0, pa0); PK4(p0, 8, pa1); PK4(p1, 0, pa2); PK4(p1, 8, pa3);
;     ...
; }
; DEVI void qkt(f32x16& p0, f32x16& p1, const char* Kb, const bf16x8 (&qr)[6], int r32, int hi, const f32x16& cinit) {
; #pragma unroll
;     for (int d0 = 0; d0 < 6; ++d0) { const int cb = (d0 * 16 + hi * 8) * 2;
;         const bf16x8 k0 = *(const bf16x8*)(Kb + KSWZ(r32, cb)), k1 = *(const bf16x8*)(Kb + KSWZ(32 + r32, cb));
;         p0 = __builtin_amdgcn_mfma_f32_32x32x16_bf16(k0, qr[d0], d0 == 0 ? cinit : p0, 0, 0, 0);
;         p1 = __builtin_amdgcn_mfma_f32_32x32x16_bf16(k1, qr[d0], d0 == 0 ? cinit : p1, 0, 0, 0); }
; }
	global_load_lds_dwordx4 v[82:83], off
	v_lshl_add_u64 v[82:83], v[120:121], 0, s[12:13]
	s_add_i32 m0, s6, 0x2000
	v_exp_f32_e32 v66, v66
	global_load_lds_dwordx4 v[82:83], off
	s_add_i32 m0, s6, 0x4000
	s_lshl_b32 s6, s61, 14
	v_lshl_add_u64 v[82:83], v[122:123], 0, s[12:13]
	s_add_i32 s6, s97, s6
	global_load_lds_dwordx4 v[82:83], off
	s_mov_b32 m0, s6
	v_lshl_add_u64 v[82:83], v[116:117], 0, s[40:41]
	global_load_lds_dwordx4 v[116:117], off
	s_add_i32 m0, s6, 0x2000
	s_mul_i32 s6, s2, 0x6000
	global_load_lds_dwordx4 v[82:83], off
	s_add_i32 s6, s6, 0
	v_add_u32_e32 v86, s6, v129
	ds_read_b128 v[82:85], v86
	ds_read_b128 v[212:215], v86 offset:6144
	s_waitcnt lgkmcnt(0)
	v_mfma_f32_32x32x16_bf16 v[98:113], v[82:85], v[150:153], v[34:49]
	v_add_u32_e32 v126, s6, v184
	v_exp_f32_e32 v67, v67
	v_exp_f32_e32 v68, v68
	v_exp_f32_e32 v69, v69
	v_exp_f32_e32 v70, v70
	v_exp_f32_e32 v71, v71
	v_exp_f32_e32 v72, v72
	v_mfma_f32_32x32x16_bf16 v[82:97], v[212:215], v[150:153], v[34:49]
	ds_read_b128 v[212:215], v126
	ds_read_b128 v[216:219], v126 offset:6144
	v_add_u32_e32 v126, s6, v185
	v_exp_f32_e32 v73, v73
	v_exp_f32_e32 v74, v74
	v_exp_f32_e32 v75, v75
	v_exp_f32_e32 v76, v76
	v_exp_f32_e32 v77, v77
	s_waitcnt lgkmcnt(0)
	v_mfma_f32_32x32x16_bf16 v[98:113], v[212:215], v[138:141], v[98:113]
	v_exp_f32_e32 v78, v78
	v_exp_f32_e32 v79, v79
	v_exp_f32_e32 v80, v80
	v_exp_f32_e32 v81, v81
	v_add_u32_e32 v174, 0x2000, v203
	v_mfma_f32_32x32x16_bf16 v[82:97], v[216:219], v[138:141], v[82:97]
	ds_read_b128 v[212:215], v126
	ds_read_b128 v[216:219], v126 offset:6144
	v_add_u32_e32 v126, s6, v205
	s_waitcnt lgkmcnt(0)
	v_mfma_f32_32x32x16_bf16 v[98:113], v[212:215], v[134:137], v[98:113]
	ds_read_b128 v[212:215], v126
	ds_read_b128 v[220:223], v126 offset:6144
	v_add_u32_e32 v126, s6, v206
	v_mfma_f32_32x32x16_bf16 v[82:97], v[216:219], v[134:137], v[82:97]
	ds_read_b128 v[216:219], v126
	ds_read_b128 v[224:227], v126 offset:6144
	v_add_u32_e32 v126, s6, v207
	ds_read_b128 v[228:231], v126
	ds_read_b128 v[232:235], v126 offset:6144
	v_pk_add_f32 v[126:127], v[50:51], v[66:67]
	v_cvt_pk_bf16_f32 v50, v50, v51
	v_cvt_pk_bf16_f32 v51, v52, v53
	s_waitcnt lgkmcnt(0)
	v_mfma_f32_32x32x16_bf16 v[98:113], v[212:215], v[130:133], v[98:113]
	v_add_f32_e64 v212, v52, v68
	v_add_f32_e64 v213, v53, v69
	v_cvt_pk_bf16_f32 v52, v54, v55
	v_cvt_pk_bf16_f32 v53, v56, v57
	v_add_f32_e64 v126, v212, v126
	v_add_f32_e64 v127, v213, v127
	v_add_f32_e64 v212, v54, v70
	v_add_f32_e64 v213, v55, v71
	v_cvt_pk_bf16_f32 v54, v58, v59
	v_mfma_f32_32x32x16_bf16 v[82:97], v[220:223], v[130:133], v[82:97]
	v_add_f32_e64 v126, v212, v126
	v_add_f32_e64 v127, v213, v127
	v_add_f32_e64 v212, v56, v72
	v_add_f32_e64 v213, v57, v73
	v_cvt_pk_bf16_f32 v55, v60, v61
	v_cvt_pk_bf16_f32 v56, v62, v63
	v_cvt_pk_bf16_f32 v57, v64, v65
	v_add_f32_e64 v126, v212, v126
	v_add_f32_e64 v127, v213, v127
	v_pk_add_f32 v[212:213], v[58:59], v[74:75]
	v_cvt_pk_bf16_f32 v58, v66, v67
	v_cvt_pk_bf16_f32 v59, v68, v69
	v_mfma_f32_32x32x16_bf16 v[98:113], v[216:219], v[146:149], v[98:113]
	v_add_f32_e64 v126, v212, v126
	v_add_f32_e64 v127, v213, v127
	v_add_f32_e64 v212, v60, v76
	v_add_f32_e64 v213, v61, v77
	v_cvt_pk_bf16_f32 v60, v70, v71
	v_cvt_pk_bf16_f32 v61, v72, v73
	v_add_f32_e64 v126, v212, v126
	v_add_f32_e64 v127, v213, v127
	v_pk_add_f32 v[212:213], v[62:63], v[78:79]
	v_cvt_pk_bf16_f32 v62, v74, v75
	v_cvt_pk_bf16_f32 v63, v76, v77
	v_mfma_f32_32x32x16_bf16 v[82:97], v[224:227], v[146:149], v[82:97]
	v_add_f32_e64 v126, v212, v126
	v_add_f32_e64 v127, v213, v127
	v_add_f32_e64 v212, v64, v80
	v_add_f32_e64 v213, v65, v81
	v_cvt_pk_bf16_f32 v64, v78, v79
	v_cvt_pk_bf16_f32 v65, v80, v81
	ds_read_b64_tr_b16 v[66:67], v174 offset:0
	ds_read_b64_tr_b16 v[68:69], v174 offset:0x400
	ds_read_b64_tr_b16 v[70:71], v174 offset:0x800
	ds_read_b64_tr_b16 v[72:73], v174 offset:0xc00
	ds_read_b64_tr_b16 v[74:75], v174 offset:0x1000
	ds_read_b64_tr_b16 v[76:77], v174 offset:0x1400
	ds_read_b64_tr_b16 v[78:79], v174 offset:0x1800
	ds_read_b64_tr_b16 v[80:81], v174 offset:0x1c00
	v_add_f32_e64 v126, v212, v126
	v_add_f32_e64 v127, v213, v127
	ds_read_b64_tr_b16 v[212:213], v174 offset:0x200
	ds_read_b64_tr_b16 v[214:215], v174 offset:0x600
	ds_read_b64_tr_b16 v[216:217], v174 offset:0xa00
	v_mfma_f32_32x32x16_bf16 v[98:113], v[228:231], v[142:145], v[98:113]
	ds_read_b64_tr_b16 v[218:219], v174 offset:0xe00
	ds_read_b64_tr_b16 v[220:221], v174 offset:0x1200
	ds_read_b64_tr_b16 v[222:223], v174 offset:0x1600
	ds_read_b64_tr_b16 v[224:225], v174 offset:0x1a00
	ds_read_b64_tr_b16 v[226:227], v174 offset:0x1e00
	v_pk_add_f32 v[126:127], v[126:127], v[126:127] op_sel:[0,1] op_sel_hi:[1,0]
	s_waitcnt lgkmcnt(8)
	v_mfma_f32_32x32x16_bf16 v[82:97], v[232:235], v[142:145], v[82:97]
	v_mov_b32_e32 v127, v126
	s_nop 1
	v_permlane32_swap_b32_e32 v126, v127
	v_mfma_f32_32x32x16_bf16 v[18:33], v[50:53], v[66:69], v[18:33]
	s_waitcnt lgkmcnt(0)
	v_mfma_f32_32x32x16_bf16 v[18:33], v[54:57], v[70:73], v[18:33]
	v_mfma_f32_32x32x16_bf16 v[18:33], v[58:61], v[74:77], v[18:33]
	v_mfma_f32_32x32x16_bf16 v[18:33], v[62:65], v[78:81], v[18:33]
	v_mfma_f32_32x32x16_bf16 v[2:17], v[50:53], v[212:215], v[2:17]
	s_nop 0
	v_max_f32_e32 v249, v99, v99
	v_max_f32_e32 v250, v98, v98
	v_max_f32_e32 v249, v250, v249
	v_max3_f32 v249, v249, v100, v101
	v_max3_f32 v249, v249, v102, v103
	v_max3_f32 v251, v249, v104, v105
	v_max3_f32 v251, v251, v106, v107
	v_exp_f32_e32 v50, v98
	v_exp_f32_e32 v51, v99
	v_exp_f32_e32 v52, v100
	v_exp_f32_e32 v53, v101
	v_mov_b64_e32 v[66:67], v[82:83]
	v_mov_b64_e32 v[68:69], v[84:85]
	v_mfma_f32_32x32x16_bf16 v[2:17], v[54:57], v[216:219], v[2:17]
	v_max3_f32 v251, v251, v108, v109
	v_max3_f32 v251, v251, v110, v111
	v_max3_f32 v251, v251, v112, v113
	v_max3_f32 v251, v251, v82, v83
	v_max3_f32 v251, v251, v84, v85
	v_max3_f32 v251, v251, v86, v87
	v_max3_f32 v251, v251, v88, v89
	v_exp_f32_e32 v54, v102
	v_exp_f32_e32 v55, v103
	v_exp_f32_e32 v56, v104
	v_exp_f32_e32 v57, v105
	v_mov_b64_e32 v[70:71], v[86:87]
	v_mov_b64_e32 v[72:73], v[88:89]
	v_mfma_f32_32x32x16_bf16 v[2:17], v[58:61], v[220:223], v[2:17]
	v_max3_f32 v251, v251, v90, v91
	v_max3_f32 v251, v251, v92, v93
	v_max3_f32 v251, v251, v94, v95
	v_max3_f32 v251, v251, v96, v97
	v_mov_b32_e32 v252, v251
	s_nop 1
	v_permlane32_swap_b32_e32 v251, v252
	v_exp_f32_e32 v58, v106
	v_exp_f32_e32 v59, v107
	v_exp_f32_e32 v60, v108
	v_exp_f32_e32 v61, v109
	v_mov_b64_e32 v[74:75], v[90:91]
	v_mov_b64_e32 v[76:77], v[92:93]
	v_mfma_f32_32x32x16_bf16 v[2:17], v[62:65], v[224:227], v[2:17]
	v_exp_f32_e32 v62, v110
	v_exp_f32_e32 v63, v111
	v_exp_f32_e32 v64, v112
	v_exp_f32_e32 v65, v113
	v_mov_b64_e32 v[78:79], v[94:95]
	v_mov_b64_e32 v[80:81], v[96:97]
	v_max_f32_e32 v252, v252, v252
	v_max_f32_e32 v251, v251, v251
	v_max_f32_e32 v174, v251, v252
	v_cmp_ge_f32_e32 vcc, s80, v174
	s_cmp_lg_u64 vcc, exec
	s_cselect_b64 s[6:7], -1, 0
	s_cbranch_scc1 .LBB0_2275
	v_mov_b32_e32 v203, 1.0
	v_mov_b32_e32 v204, v210
	s_branch .LBB0_2280

; template <bool FIRST> DEVI bool partialSM(f32x16& p0, f32x16& p1, float& m_reg, float& alpha) {
;     ...
;     } else { const float d = fmaxf(pmax, 0.f); alpha = __builtin_amdgcn_exp2f(-d); m_reg += d;
; #pragma unroll
;         for (int r = 0; r < 16; ++r) { p0[r] = __builtin_amdgcn_exp2f(p0[r] - d); p1[r] = p1[r] - d; }
;         return true;
;     }
.LBB0_2269:
	v_max_f32_e32 v50, v126, v126
	v_max_f32_e32 v66, 0, v50
	v_sub_f32_e32 v50, v98, v66
	v_sub_f32_e32 v51, v99, v66
	v_sub_f32_e32 v52, v100, v66
	v_sub_f32_e32 v53, v101, v66
	v_sub_f32_e32 v54, v102, v66
	v_sub_f32_e32 v55, v103, v66
	v_sub_f32_e32 v56, v104, v66
	v_sub_f32_e32 v57, v105, v66
	v_sub_f32_e32 v58, v106, v66
	v_sub_f32_e32 v59, v107, v66
	v_sub_f32_e32 v60, v108, v66
	v_sub_f32_e32 v61, v109, v66
	v_sub_f32_e32 v62, v110, v66
	v_sub_f32_e32 v63, v111, v66
	v_sub_f32_e32 v64, v112, v66
	v_sub_f32_e32 v65, v113, v66
	v_exp_f32_e64 v209, -v66
	v_add_f32_e32 v210, v204, v66
	v_exp_f32_e32 v50, v50
	v_exp_f32_e32 v51, v51
	v_exp_f32_e32 v52, v52
	v_exp_f32_e32 v53, v53
	v_exp_f32_e32 v54, v54
	v_exp_f32_e32 v55, v55
	v_exp_f32_e32 v56, v56
	v_exp_f32_e32 v57, v57
	v_exp_f32_e32 v58, v58
	v_exp_f32_e32 v59, v59
	v_exp_f32_e32 v60, v60
	v_exp_f32_e32 v61, v61
	v_exp_f32_e32 v62, v62
	v_exp_f32_e32 v63, v63
	v_exp_f32_e32 v64, v64
	v_exp_f32_e32 v65, v65
	v_sub_f32_e32 v81, v97, v66
	v_sub_f32_e32 v80, v96, v66
	v_sub_f32_e32 v79, v95, v66
	v_sub_f32_e32 v78, v94, v66
	v_sub_f32_e32 v77, v93, v66
	v_sub_f32_e32 v76, v92, v66
	v_sub_f32_e32 v75, v91, v66
	v_sub_f32_e32 v74, v90, v66
	v_sub_f32_e32 v73, v89, v66
	v_sub_f32_e32 v72, v88, v66
	v_sub_f32_e32 v71, v87, v66
	v_sub_f32_e32 v70, v86, v66
	v_sub_f32_e32 v69, v85, v66
	v_sub_f32_e32 v68, v84, v66
	v_sub_f32_e32 v67, v83, v66
	v_sub_f32_e32 v66, v82, v66
	s_cbranch_execnz .LBB0_2262
.LBB0_2271:
	s_and_saveexec_b64 s[6:7], s[4:5]
	ds_write_b32 v188, v209 offset:128
	s_or_b64 exec, exec, s[6:7]
	v_add_u32_e32 v46, s93, v178
	s_waitcnt lgkmcnt(0)
	ds_read_b128 v[34:37], v46 offset:224
	ds_read_b128 v[38:41], v46 offset:192
	ds_read_b128 v[42:45], v46 offset:160
	ds_read_b128 v[46:49], v46 offset:128
	s_waitcnt lgkmcnt(0)
	v_pk_mul_f32 v[30:31], v[30:31], v[34:35]
	v_pk_mul_f32 v[14:15], v[14:15], v[34:35]
	v_xor_b32_e32 v34, 0x80000000, v210
	s_waitcnt lgkmcnt(2)
	v_pk_mul_f32 v[26:27], v[26:27], v[38:39]
	s_waitcnt lgkmcnt(1)
	v_pk_mul_f32 v[22:23], v[22:23], v[42:43]
	v_pk_mul_f32 v[32:33], v[32:33], v[36:37]
	v_pk_mul_f32 v[28:29], v[28:29], v[40:41]
	v_pk_mul_f32 v[24:25], v[24:25], v[44:45]
	s_waitcnt lgkmcnt(0)
	v_pk_mul_f32 v[20:21], v[20:21], v[48:49]
	v_pk_mul_f32 v[18:19], v[18:19], v[46:47]
	v_pk_mul_f32 v[10:11], v[10:11], v[38:39]
	v_pk_mul_f32 v[6:7], v[6:7], v[42:43]
	v_pk_mul_f32 v[16:17], v[16:17], v[36:37]
	v_pk_mul_f32 v[12:13], v[12:13], v[40:41]
	v_pk_mul_f32 v[8:9], v[8:9], v[44:45]
	v_pk_mul_f32 v[4:5], v[4:5], v[48:49]
	v_pk_mul_f32 v[2:3], v[2:3], v[46:47]
	v_mov_b32_e32 v35, v34
	v_mov_b32_e32 v36, v34
	v_mov_b32_e32 v37, v34
	v_mov_b32_e32 v38, v34
	v_mov_b32_e32 v39, v34
	v_mov_b32_e32 v40, v34
	v_mov_b32_e32 v41, v34
	v_mov_b32_e32 v42, v34
	v_mov_b32_e32 v43, v34
	v_mov_b32_e32 v44, v34
	v_mov_b32_e32 v45, v34
	v_mov_b32_e32 v46, v34
	v_mov_b32_e32 v47, v34
	v_mov_b32_e32 v48, v34
	v_mov_b32_e32 v49, v34
	s_andn2_b64 vcc, exec, s[14:15]
	s_mov_b64 s[6:7], -1
	s_cbranch_vccnz .LBB0_2264

; template <bool FIRST> DEVI bool partialSM(f32x16& p0, f32x16& p1, float& m_reg, float& alpha) {
;     ...
;     } else { const float d = fmaxf(pmax, 0.f); alpha = __builtin_amdgcn_exp2f(-d); m_reg += d;
; #pragma unroll
;         for (int r = 0; r < 16; ++r) { p0[r] = __builtin_amdgcn_exp2f(p0[r] - d); p1[r] = p1[r] - d; }
;         return true;
;     }
.LBB0_2275:
	v_max_f32_e32 v50, v174, v174
	v_max_f32_e32 v66, 0, v50
	v_sub_f32_e32 v50, v98, v66
	v_sub_f32_e32 v51, v99, v66
	v_sub_f32_e32 v52, v100, v66
	v_sub_f32_e32 v53, v101, v66
	v_sub_f32_e32 v54, v102, v66
	v_sub_f32_e32 v55, v103, v66
	v_sub_f32_e32 v56, v104, v66
	v_sub_f32_e32 v57, v105, v66
	v_sub_f32_e32 v58, v106, v66
	v_sub_f32_e32 v59, v107, v66
	v_sub_f32_e32 v60, v108, v66
	v_sub_f32_e32 v61, v109, v66
	v_sub_f32_e32 v62, v110, v66
	v_sub_f32_e32 v63, v111, v66
	v_sub_f32_e32 v64, v112, v66
	v_sub_f32_e32 v65, v113, v66
	v_exp_f32_e64 v203, -v66
	v_add_f32_e32 v204, v210, v66
	v_exp_f32_e32 v50, v50
	v_exp_f32_e32 v51, v51
	v_exp_f32_e32 v52, v52
	v_exp_f32_e32 v53, v53
	v_exp_f32_e32 v54, v54
	v_exp_f32_e32 v55, v55
	v_exp_f32_e32 v56, v56
	v_exp_f32_e32 v57, v57
	v_exp_f32_e32 v58, v58
	v_exp_f32_e32 v59, v59
	v_exp_f32_e32 v60, v60
	v_exp_f32_e32 v61, v61
	v_exp_f32_e32 v62, v62
	v_exp_f32_e32 v63, v63
	v_exp_f32_e32 v64, v64
	v_exp_f32_e32 v65, v65
	v_sub_f32_e32 v81, v97, v66
	v_sub_f32_e32 v80, v96, v66
	v_sub_f32_e32 v79, v95, v66
	v_sub_f32_e32 v78, v94, v66
	v_sub_f32_e32 v77, v93, v66
	v_sub_f32_e32 v76, v92, v66
	v_sub_f32_e32 v75, v91, v66
	v_sub_f32_e32 v74, v90, v66
	v_sub_f32_e32 v73, v89, v66
	v_sub_f32_e32 v72, v88, v66
	v_sub_f32_e32 v71, v87, v66
	v_sub_f32_e32 v70, v86, v66
	v_sub_f32_e32 v69, v85, v66
	v_sub_f32_e32 v68, v84, v66
	v_sub_f32_e32 v67, v83, v66
	v_sub_f32_e32 v66, v82, v66
	s_cbranch_execnz .LBB0_2268
.LBB0_2277:
	s_and_saveexec_b64 s[6:7], s[4:5]
	ds_write_b32 v188, v203 offset:128
	s_or_b64 exec, exec, s[6:7]
	v_add_u32_e32 v46, s93, v178
	s_waitcnt lgkmcnt(0)
	ds_read_b128 v[34:37], v46 offset:224
	ds_read_b128 v[38:41], v46 offset:192
	ds_read_b128 v[42:45], v46 offset:160
	ds_read_b128 v[46:49], v46 offset:128
	s_waitcnt lgkmcnt(0)
	v_pk_mul_f32 v[30:31], v[30:31], v[34:35]
	v_pk_mul_f32 v[14:15], v[14:15], v[34:35]
	v_xor_b32_e32 v34, 0x80000000, v204
	v_pk_mul_f32 v[26:27], v[26:27], v[38:39]
	v_pk_mul_f32 v[22:23], v[22:23], v[42:43]
	v_pk_mul_f32 v[32:33], v[32:33], v[36:37]
	v_pk_mul_f32 v[28:29], v[28:29], v[40:41]
	v_pk_mul_f32 v[24:25], v[24:25], v[44:45]
	v_pk_mul_f32 v[20:21], v[20:21], v[48:49]
	v_pk_mul_f32 v[18:19], v[18:19], v[46:47]
	v_pk_mul_f32 v[10:11], v[10:11], v[38:39]
	v_pk_mul_f32 v[6:7], v[6:7], v[42:43]
	v_pk_mul_f32 v[16:17], v[16:17], v[36:37]
	v_pk_mul_f32 v[12:13], v[12:13], v[40:41]
	v_pk_mul_f32 v[8:9], v[8:9], v[44:45]
	v_pk_mul_f32 v[4:5], v[4:5], v[48:49]
	v_pk_mul_f32 v[2:3], v[2:3], v[46:47]
	v_mov_b32_e32 v35, v34
	v_mov_b32_e32 v36, v34
	v_mov_b32_e32 v37, v34
	v_mov_b32_e32 v38, v34
	v_mov_b32_e32 v39, v34
	v_mov_b32_e32 v40, v34
	v_mov_b32_e32 v41, v34
	v_mov_b32_e32 v42, v34
	v_mov_b32_e32 v43, v34
	v_mov_b32_e32 v44, v34
	v_mov_b32_e32 v45, v34
	v_mov_b32_e32 v46, v34
	v_mov_b32_e32 v47, v34
	v_mov_b32_e32 v48, v34
	v_mov_b32_e32 v49, v34

; #define LAS __attribute__((address_space(3)))
; #define PHASE(PH, L) do { run_phase<PH>(fresh_params(), smem, L); } while (0)
; #define GRID_BARRIER() do { XcdBarrier b_; b_.bar = fresh_params().bar; b_.x = xb_xcc_id(); b_.st = (volatile LAS unsigned*)(LAS char*)(smem + LDS_BYTES - 16); xcd_barrier(b_); } while (0)
; #define LAYER(l, LAST) do { PHASE_B(2, l); PHASE_B(3, l); PHASE_B(4, l); PHASE_B(5, l); PHASE_B(6, l); PHASE_B(7, l); PHASE_B(8, l); PHASE_B(9, l); PHASE(15, l); GRID_BARRIER(); PHASE_B(11, l); PHASE_B(12, l); \
;         PHASE(13, l); if (!(LAST)) GRID_BARRIER(); \
;         if (DUP_MASK & (1 << 13)) { GRID_BARRIER(); PHASE(13, l); GRID_BARRIER(); } } while (0)
; __global__ void __launch_bounds__(512, 2) k_mega(Params p_unused) {
;     extern __shared__ __attribute__((aligned(16))) char smem[];
;     { volatile LAS unsigned* xbw = (volatile LAS unsigned*)(LAS char*)(smem + LDS_BYTES - 16);
;       if (threadIdx.x == 0) { xbw[0] = 0u; xbw[1] = 0u; xbw[2] = 0u; xbw[3] = 0u; }
;       __syncthreads();
;       (void)xcd_barrier_post(fresh_params().bar, xbw); }
;     PHASE(0, 0); GRID_BARRIER(); if (DUP_MASK & 1) { PHASE(0, 0); GRID_BARRIER(); }
;     PHASE(1, 0); GRID_BARRIER(); if (DUP_MASK & 2) { PHASE(1, 0); GRID_BARRIER(); }
;     ...
;     LAYER(0, false);
;     LAYER(1, true);
; }
	.amdhsa_kernel _Z6k_mega6Params
		.amdhsa_group_segment_fixed_size 0
		.amdhsa_private_segment_fixed_size 0
		.amdhsa_kernarg_size 816
		.amdhsa_user_sgpr_count 2
		.amdhsa_user_sgpr_dispatch_ptr 0
		.amdhsa_user_sgpr_queue_ptr 0
		.amdhsa_user_sgpr_kernarg_segment_ptr 1
		.amdhsa_user_sgpr_dispatch_id 0
		.amdhsa_user_sgpr_kernarg_preload_length 0
		.amdhsa_user_sgpr_kernarg_preload_offset 0
		.amdhsa_user_sgpr_private_segment_size 0
		.amdhsa_uses_dynamic_stack 0
		.amdhsa_enable_private_segment 0
		.amdhsa_system_sgpr_workgroup_id_x 1
		.amdhsa_system_sgpr_workgroup_id_y 0
		.amdhsa_system_sgpr_workgroup_id_z 0
		.amdhsa_system_sgpr_workgroup_info 0
		.amdhsa_system_vgpr_workitem_id 0
		.amdhsa_next_free_vgpr 256
		.amdhsa_next_free_sgpr 98
		.amdhsa_accum_offset 256
		.amdhsa_reserve_vcc 1
		.amdhsa_float_round_mode_32 0
		.amdhsa_float_round_mode_16_64 0
		.amdhsa_float_denorm_mode_32 3
		.amdhsa_float_denorm_mode_16_64 3
		.amdhsa_dx10_clamp 1
		.amdhsa_ieee_mode 1
		.amdhsa_fp16_overflow 0
		.amdhsa_tg_split 0
		.amdhsa_exception_fp_ieee_invalid_op 0
		.amdhsa_exception_fp_denorm_src 0
		.amdhsa_exception_fp_ieee_div_zero 0
		.amdhsa_exception_fp_ieee_overflow 0
		.amdhsa_exception_fp_ieee_underflow 0
		.amdhsa_exception_fp_ieee_inexact 0
		.amdhsa_exception_int_div_zero 0
	.end_amdhsa_kernel

; #define LAS __attribute__((address_space(3)))
; #define PHASE(PH, L) do { run_phase<PH>(fresh_params(), smem, L); } while (0)
; #define GRID_BARRIER() do { XcdBarrier b_; b_.bar = fresh_params().bar; b_.x = xb_xcc_id(); b_.st = (volatile LAS unsigned*)(LAS char*)(smem + LDS_BYTES - 16); xcd_barrier(b_); } while (0)
; #define LAYER(l, LAST) do { PHASE_B(2, l); PHASE_B(3, l); PHASE_B(4, l); PHASE_B(5, l); PHASE_B(6, l); PHASE_B(7, l); PHASE_B(8, l); PHASE_B(9, l); PHASE(15, l); GRID_BARRIER(); PHASE_B(11, l); PHASE_B(12, l); \
;         PHASE(13, l); if (!(LAST)) GRID_BARRIER(); \
;         if (DUP_MASK & (1 << 13)) { GRID_BARRIER(); PHASE(13, l); GRID_BARRIER(); } } while (0)
; __global__ void __launch_bounds__(512, 2) k_mega(Params p_unused) {
;     extern __shared__ __attribute__((aligned(16))) char smem[];
;     { volatile LAS unsigned* xbw = (volatile LAS unsigned*)(LAS char*)(smem + LDS_BYTES - 16);
;       if (threadIdx.x == 0) { xbw[0] = 0u; xbw[1] = 0u; xbw[2] = 0u; xbw[3] = 0u; }
;       __syncthreads();
;       (void)xcd_barrier_post(fresh_params().bar, xbw); }
;     PHASE(0, 0); GRID_BARRIER(); if (DUP_MASK & 1) { PHASE(0, 0); GRID_BARRIER(); }
;     PHASE(1, 0); GRID_BARRIER(); if (DUP_MASK & 2) { PHASE(1, 0); GRID_BARRIER(); }
;     ...
;     LAYER(0, false);
;     LAYER(1, true);
; }
.Lfunc_end0:
	.size	_Z6k_mega6Params, .Lfunc_end0-_Z6k_mega6Params
	.set _Z6k_mega6Params.num_vgpr, 256
	.set _Z6k_mega6Params.num_agpr, 0
	.set _Z6k_mega6Params.numbered_sgpr, 98
	.set _Z6k_mega6Params.num_named_barrier, 0
	.set _Z6k_mega6Params.private_seg_size, 0
	.set _Z6k_mega6Params.uses_vcc, 1
	.set _Z6k_mega6Params.uses_flat_scratch, 0
	.set _Z6k_mega6Params.has_dyn_sized_stack, 0
	.set _Z6k_mega6Params.has_recursion, 0
	.set _Z6k_mega6Params.has_indirect_call, 0

; #define LAS __attribute__((address_space(3)))
; #define PHASE(PH, L) do { run_phase<PH>(fresh_params(), smem, L); } while (0)
; #define GRID_BARRIER() do { XcdBarrier b_; b_.bar = fresh_params().bar; b_.x = xb_xcc_id(); b_.st = (volatile LAS unsigned*)(LAS char*)(smem + LDS_BYTES - 16); xcd_barrier(b_); } while (0)
; #define LAYER(l, LAST) do { PHASE_B(2, l); PHASE_B(3, l); PHASE_B(4, l); PHASE_B(5, l); PHASE_B(6, l); PHASE_B(7, l); PHASE_B(8, l); PHASE_B(9, l); PHASE(15, l); GRID_BARRIER(); PHASE_B(11, l); PHASE_B(12, l); \
;         PHASE(13, l); if (!(LAST)) GRID_BARRIER(); \
;         if (DUP_MASK & (1 << 13)) { GRID_BARRIER(); PHASE(13, l); GRID_BARRIER(); } } while (0)
; __global__ void __launch_bounds__(512, 2) k_mega(Params p_unused) {
;     extern __shared__ __attribute__((aligned(16))) char smem[];
;     { volatile LAS unsigned* xbw = (volatile LAS unsigned*)(LAS char*)(smem + LDS_BYTES - 16);
;       if (threadIdx.x == 0) { xbw[0] = 0u; xbw[1] = 0u; xbw[2] = 0u; xbw[3] = 0u; }
;       __syncthreads();
;       (void)xcd_barrier_post(fresh_params().bar, xbw); }
;     PHASE(0, 0); GRID_BARRIER(); if (DUP_MASK & 1) { PHASE(0, 0); GRID_BARRIER(); }
;     PHASE(1, 0); GRID_BARRIER(); if (DUP_MASK & 2) { PHASE(1, 0); GRID_BARRIER(); }
;     ...
;     LAYER(0, false);
;     LAYER(1, true);
; }
amdhsa.kernels:
  - .agpr_count:     0
    .args:
      - .offset:         0
        .size:           560
        .value_kind:     by_value
      - .offset:         560
        .size:           4
        .value_kind:     hidden_block_count_x
      - .offset:         564
        .size:           4
        .value_kind:     hidden_block_count_y
      - .offset:         568
        .size:           4
        .value_kind:     hidden_block_count_z
      - .offset:         572
        .size:           2
        .value_kind:     hidden_group_size_x
      - .offset:         574
        .size:           2
        .value_kind:     hidden_group_size_y
      - .offset:         576
        .size:           2
        .value_kind:     hidden_group_size_z
      - .offset:         578
        .size:           2
        .value_kind:     hidden_remainder_x
      - .offset:         580
        .size:           2
        .value_kind:     hidden_remainder_y
      - .offset:         582
        .size:           2
        .value_kind:     hidden_remainder_z
      - .offset:         600
        .size:           8
        .value_kind:     hidden_global_offset_x
      - .offset:         608
        .size:           8
        .value_kind:     hidden_global_offset_y
      - .offset:         616
        .size:           8
        .value_kind:     hidden_global_offset_z
      - .offset:         624
        .size:           2
        .value_kind:     hidden_grid_dims
      - .offset:         680
        .size:           4
        .value_kind:     hidden_dynamic_lds_size
    .group_segment_fixed_size: 0
    .kernarg_segment_align: 8
    .kernarg_segment_size: 816
    .language:       OpenCL C
    .language_version:
      - 2
      - 0
    .max_flat_workgroup_size: 512
    .name:           _Z6k_mega6Params
    .private_segment_fixed_size: 0
    .sgpr_count:     104
    .sgpr_spill_count: 9
    .symbol:         _Z6k_mega6Params.kd
    .uniform_work_group_size: 1
    .uses_dynamic_stack: false
    .vgpr_count:     256
    .vgpr_spill_count: 0
    .wavefront_size: 64
